# v11 + P0: static priority raise for waves 0..3 (reset at P1 entry)
# baseline (speedup 1.0000x reference)
.LBB0_13:
	v_writelane_b32 v254, s8, 3
	s_load_dwordx16 s[52:67], s[0:1], 0x40
	s_cmp_lt_i32 s92, 1
	v_writelane_b32 v254, s9, 4
	v_writelane_b32 v254, s10, 5
	v_writelane_b32 v254, s11, 6
	v_writelane_b32 v254, s12, 7
	v_writelane_b32 v254, s13, 8
	v_writelane_b32 v254, s14, 9
	v_writelane_b32 v254, s15, 10
	v_writelane_b32 v254, s16, 11
	v_writelane_b32 v254, s17, 12
	v_writelane_b32 v254, s18, 13
	v_writelane_b32 v254, s19, 14
	v_writelane_b32 v254, s20, 15
	v_writelane_b32 v254, s21, 16
	v_writelane_b32 v254, s22, 17
	v_writelane_b32 v254, s23, 18
	s_load_dwordx16 s[4:19], s[0:1], 0x0
	s_cselect_b64 s[0:1], -1, 0
	s_cmp_gt_i32 s93, 0
	s_cselect_b64 s[2:3], -1, 0
	s_and_b64 s[0:1], s[0:1], s[2:3]
	s_waitcnt lgkmcnt(0)
	v_writelane_b32 v254, s4, 19
	s_andn2_b64 vcc, exec, s[0:1]
	s_nop 0
	v_writelane_b32 v254, s5, 20
	v_writelane_b32 v254, s6, 21
	v_writelane_b32 v254, s7, 22
	v_writelane_b32 v254, s8, 23
	v_writelane_b32 v254, s9, 24
	v_writelane_b32 v254, s10, 25
	v_writelane_b32 v254, s11, 26
	v_writelane_b32 v254, s12, 27
	v_writelane_b32 v254, s13, 28
	v_writelane_b32 v254, s14, 29
	v_writelane_b32 v254, s15, 30
	v_writelane_b32 v254, s16, 31
	v_writelane_b32 v254, s17, 32
	v_writelane_b32 v254, s18, 33
	v_writelane_b32 v254, s19, 34
	v_writelane_b32 v254, s70, 35
	s_cbranch_vccnz .LBB0_253
	v_readfirstlane_b32 s98, v0
	s_bitcmp1_b32 s98, 8
	s_cbranch_scc1 .Lp0_noprio
	s_setprio 1
.Lp0_noprio:
	v_mov_b32_e32 v26, v0
	s_movk_i32 s0, 0x1000
	s_nop 0
	v_readfirstlane_b32 s2, v26
	v_cmp_gt_i32_e32 vcc, s0, v26
	v_lshl_add_u32 v1, v26, 2, 0
	s_and_saveexec_b64 s[0:1], vcc
	s_cbranch_execz .LBB0_17
	v_readlane_b32 s4, v254, 19
	v_readlane_b32 s6, v254, 21
	v_readlane_b32 s7, v254, 22
	v_readlane_b32 s5, v254, 20
	v_mov_b32_e32 v2, s6
	v_mov_b32_e32 v3, s7
	v_ashrrev_i32_e32 v27, 31, v26
	v_add_u32_e32 v4, 0x2000, v1
	v_add_u32_e32 v5, 0xfffffe00, v26
	v_lshl_add_u64 v[2:3], v[26:27], 2, v[2:3]
	s_mov_b64 s[4:5], 0
	s_mov_b64 s[6:7], 0x800
	s_movk_i32 s3, 0xdff
	v_readlane_b32 s8, v254, 23
	v_readlane_b32 s9, v254, 24
	v_readlane_b32 s10, v254, 25
	v_readlane_b32 s11, v254, 26
	v_readlane_b32 s12, v254, 27
	v_readlane_b32 s13, v254, 28
	v_readlane_b32 s14, v254, 29
	v_readlane_b32 s15, v254, 30
	v_readlane_b32 s16, v254, 31
	v_readlane_b32 s17, v254, 32
	v_readlane_b32 s18, v254, 33
	v_readlane_b32 s19, v254, 34

.LBB0_253:
	s_setprio 0
	s_cmp_lt_i32 s92, 2
	s_cselect_b64 s[0:1], -1, 0
	s_cmp_gt_i32 s93, 1
	s_cselect_b64 s[2:3], -1, 0
	s_and_b64 s[0:1], s[0:1], s[2:3]
	s_andn2_b64 vcc, exec, s[0:1]
	s_cbranch_vccnz .LBB0_313
	s_waitcnt vmcnt(15)
	v_mov_b32_e32 v26, v0
	s_ashr_i32 s91, s90, 31
	s_lshl_b64 s[22:23], s[90:91], 9
	v_ashrrev_i32_e32 v27, 31, v26
	v_lshl_add_u64 v[10:11], s[22:23], 0, v[26:27]
	s_mov_b64 s[4:5], 0x400000
	v_cmp_gt_u64_e32 vcc, s[4:5], v[10:11]
	s_and_saveexec_b64 s[6:7], vcc
	s_cbranch_execz .LBB0_263
	v_lshlrev_b32_e32 v2, 3, v26
	v_readlane_b32 s36, v254, 3
	v_ashrrev_i32_e32 v3, 31, v2
	v_readlane_b32 s50, v254, 17
	v_readlane_b32 s51, v254, 18
	s_mov_b64 s[0:1], 0x100000
	s_ashr_i32 s85, s84, 31
	v_lshl_add_u64 v[2:3], v[2:3], 2, s[50:51]
	v_lshl_add_u64 v[12:13], v[2:3], 0, s[0:1]
	v_add_co_u32_e32 v14, vcc, 0x100000, v2
	s_mov_b64 s[0:1], 0x104000
	v_lshl_add_u64 v[4:5], v[2:3], 0, s[0:1]
	s_mov_b64 s[0:1], vcc
	v_add_co_u32_e32 v6, vcc, 0x104000, v2
	v_readlane_b32 s38, v254, 5
	s_nop 0
	v_addc_co_u32_e32 v7, vcc, 0, v3, vcc
	global_load_dwordx4 v[32:35], v[6:7], off
	global_load_dwordx4 v[36:39], v[4:5], off offset:16
	v_addc_co_u32_e64 v15, vcc, 0, v3, s[0:1]
	global_load_dwordx4 v[2:5], v[14:15], off
	global_load_dwordx4 v[6:9], v[12:13], off offset:16
	s_lshl_b64 s[12:13], s[84:85], 9
	s_lshl_b64 s[14:15], s[84:85], 10
	v_readlane_b32 s39, v254, 6
	s_add_u32 s38, s14, s22
	s_mul_i32 s0, s84, 0x600
	s_addc_u32 s39, s15, s23
	s_lshl_b64 s[68:69], s[84:85], 15
	s_lshl_b64 s[72:73], s[84:85], 14
	s_mul_hi_i32 s1, s84, 0x600
	v_lshl_add_u64 v[14:15], s[38:39], 0, v[26:27]
	s_add_u32 s38, s0, s22
	s_addc_u32 s39, s1, s23
	v_readlane_b32 s40, v254, 7
	v_readlane_b32 s41, v254, 8
	v_readlane_b32 s42, v254, 9
	v_readlane_b32 s43, v254, 10
	v_readlane_b32 s44, v254, 11
	v_readlane_b32 s45, v254, 12
	v_readlane_b32 s46, v254, 13
	v_readlane_b32 s47, v254, 14
	v_readlane_b32 s48, v254, 15
	v_readlane_b32 s49, v254, 16
	s_add_u32 s22, s22, s12
	v_lshl_add_u64 v[18:19], s[38:39], 0, v[26:27]
	s_addc_u32 s23, s23, s13
	s_lshl_b64 s[38:39], s[90:91], 14
	v_readlane_b32 s40, v254, 19
	v_readlane_b32 s41, v254, 20
	v_readlane_b32 s42, v254, 21
	v_readlane_b32 s43, v254, 22
	s_add_u32 s38, s40, s38
	v_readlane_b32 s37, v254, 4
	v_mov_b64_e32 v[20:21], 0x25f00000
	v_mov_b64_e32 v[22:23], 0x1f700000
	v_lshl_add_u64 v[28:29], s[22:23], 0, v[26:27]
	s_addc_u32 s39, s41, s39
	s_lshl_b64 s[40:41], s[90:91], 13
	s_lshl_b64 s[42:43], s[90:91], 12
	s_mov_b64 s[34:35], 0x25f00000
	s_mov_b64 s[36:37], 0x1f700000
	v_lshlrev_b64 v[24:25], 5, v[26:27]
	v_lshl_add_u64 v[12:13], v[14:15], 4, v[20:21]
	v_lshl_add_u64 v[14:15], v[14:15], 3, v[22:23]
	v_lshl_add_u64 v[16:17], v[18:19], 4, v[20:21]
	v_lshl_add_u64 v[18:19], v[18:19], 3, v[22:23]
	v_lshl_add_u64 v[20:21], v[28:29], 4, v[20:21]
	v_lshl_add_u64 v[22:23], v[28:29], 3, v[22:23]
	v_lshl_add_u64 v[28:29], v[26:27], 4, s[40:41]
	s_waitcnt vmcnt(18)
	v_lshl_add_u64 v[30:31], v[26:27], 3, s[42:43]
	s_mov_b64 s[8:9], 0
	s_mov_b32 s2, 0xc3e00000
	s_mov_b64 s[10:11], 0x3fffff
	s_lshl_b64 s[74:75], s[84:85], 16
	v_lshl_add_u64 v[24:25], s[38:39], 0, v[24:25]
	v_lshl_add_u64 v[26:27], v[28:29], 0, s[34:35]
	v_lshl_add_u64 v[28:29], v[30:31], 0, s[36:37]
	v_mov_b32_e32 v1, 0x43e00000
	v_readlane_b32 s44, v254, 23
	v_readlane_b32 s45, v254, 24
	v_readlane_b32 s46, v254, 25
	v_readlane_b32 s47, v254, 26
	v_readlane_b32 s48, v254, 27
	v_readlane_b32 s49, v254, 28
	v_readlane_b32 s50, v254, 29
	v_readlane_b32 s51, v254, 30
	v_readlane_b32 s52, v254, 31
	v_readlane_b32 s53, v254, 32
	v_readlane_b32 s54, v254, 33
	v_readlane_b32 s55, v254, 34
	s_waitcnt vmcnt(3)
	v_pk_add_f32 v[30:31], v[34:35], 1.0 op_sel_hi:[1,0]
	v_pk_add_f32 v[32:33], v[32:33], 1.0 op_sel_hi:[1,0]
	s_waitcnt vmcnt(2)
	v_pk_add_f32 v[34:35], v[38:39], 1.0 op_sel_hi:[1,0]
	v_pk_add_f32 v[36:37], v[36:37], 1.0 op_sel_hi:[1,0]
	s_branch .LBB0_259
